# expert-weight conversion group staggered across workgroups: dealt at trip == (bid>>3)&3 instead of trip%3==2 everywhere
# speedup vs baseline: 1.0025x; 1.0017x over previous
;     ...
;     for (int trip = 0;; ++trip) {
;         if (!conv_done && (att_done || (trip % 3) == 2)) {
;             __syncthreads();
;             if (F.tid == 0) CTL[2] = __hip_atomic_fetch_add(qctr + 16, 1u, __ATOMIC_RELAXED, __HIP_MEMORY_SCOPE_AGENT);
;             __syncthreads();
;             const int cu = (int)CTL[2];
;             if (cu >= CONV_UNITS) conv_done = true; else conv_experts_items(F, l, cu * CONV_GROUP, (cu + 1) * CONV_GROUP, 1);
.LBB0_1789:
	s_mov_b64 s[0:1], -1
	s_and_b64 vcc, exec, s[50:51]
	s_mov_b64 s[50:51], -1
	s_cbranch_vccnz .LBB0_1857
	s_bfe_u32 s2, s88, 0x20003
	s_cmp_eq_u32 s79, s2
	s_cselect_b64 s[2:3], -1, 0
	s_or_b64 s[2:3], s[48:49], s[2:3]
	s_andn2_b64 vcc, exec, s[2:3]
	s_mov_b64 s[50:51], 0
	s_cbranch_vccnz .LBB0_1857
	s_waitcnt lgkmcnt(0)
	s_barrier
	s_and_saveexec_b64 s[2:3], s[8:9]
	s_cbranch_execz .LBB0_1795
	s_mov_b64 s[6:7], exec
	v_mbcnt_lo_u32_b32 v0, s6, 0
	v_mbcnt_hi_u32_b32 v0, s7, v0
	v_cmp_eq_u32_e32 vcc, 0, v0
	s_and_saveexec_b64 s[4:5], vcc
	s_cbranch_execz .LBB0_1794
	s_bcnt1_i32_b64 s6, s[6:7]
	v_mov_b32_e32 v1, s6
	global_atomic_add v1, v65, v1, s[38:39] offset:64 sc0
